# baseline (speedup 1.0000x reference)
.LBB1_93:
	s_waitcnt vmcnt(0)
	v_mfma_scale_f32_32x32x64_f8f6f4 v[2:17], v[58:65], v[98:105], v[2:17], v201, v201 op_sel_hi:[0,0,0]
	v_lshlrev_b32_e32 v18, 7, v196
	s_waitcnt lgkmcnt(0)
	s_barrier
	ds_read_b128 v[162:165], v18 offset:37376
	ds_read_b128 v[166:169], v18 offset:37392
	ds_read_b128 v[170:173], v18 offset:37408
	ds_read_b128 v[174:177], v18 offset:37424
	ds_read_b128 v[178:181], v18 offset:37440
	ds_read_b128 v[182:185], v18 offset:37456
	ds_read_b128 v[186:189], v18 offset:37472
	ds_read_b128 v[190:193], v18 offset:37488
	s_lshl_b32 s34, s35, 3
	v_or_b32_e32 v202, 0x9100, v18
	s_add_i32 s38, s34, 16
	v_mov_b32_e32 v201, 0
	s_mov_b32 s39, -2
	v_mov_b32_e32 v203, 0x7f7f7f7f
	s_add_i32 s34, s35, 1
	s_and_b32 s34, s34, 15
	s_lshl_b32 s34, s34, 3
	s_add_i32 s34, s34, s52
	s_lshl_b32 s34, s34, 13
	s_add_i32 s34, s34, s53
	buffer_load_dwordx4 v[146:149], v195, s[44:47], s34 offen
	s_or_b32 s42, s34, 0x400
	buffer_load_dwordx4 v[150:153], v195, s[44:47], s42 offen
	s_or_b32 s43, s34, 0x800
	buffer_load_dwordx4 v[154:157], v195, s[44:47], s43 offen
	s_or_b32 s42, s34, 0xc00
	buffer_load_dwordx4 v[158:161], v195, s[44:47], s42 offen
	s_or_b32 s43, s34, 0x1000
	buffer_load_dwordx4 v[138:141], v195, s[44:47], s43 offen
	s_or_b32 s42, s34, 0x1400
	buffer_load_dwordx4 v[142:145], v195, s[44:47], s42 offen
	s_or_b32 s43, s34, 0x1800
	buffer_load_dwordx4 v[130:133], v195, s[44:47], s43 offen
	s_or_b32 s42, s34, 0x1c00
	buffer_load_dwordx4 v[134:137], v195, s[44:47], s42 offen
	s_mov_b32 s39, 0
.Lq2_loop:
	s_lshl_b32 s34, s39, 2
	s_add_i32 s34, s34, s35
	s_and_b32 s41, s34, 15
	s_add_i32 s54, s34, 1
	s_and_b32 s54, s54, 15
	s_lshl_b32 s55, s41, 8
	s_lshl_b32 s38, s52, 12
	s_add_i32 s55, s55, s38
	v_lshl_add_u32 v236, v194, 2, s55
	ds_read_b32 v200, v236
	s_lshl_b32 s55, s41, 3
	s_add_i32 s55, s55, s52
	s_cmp_lg_u32 s55, s33
	s_cbranch_scc1 .Lq2_nd0_0
	v_cndmask_b32_e64 v2, v2, v198, s[0:1]
	v_cndmask_b32_e64 v3, v3, v198, s[2:3]
	v_cndmask_b32_e64 v4, v4, v198, s[4:5]
	v_cndmask_b32_e64 v5, v5, v198, s[6:7]
	v_cndmask_b32_e64 v6, v6, v198, s[8:9]
	v_cndmask_b32_e64 v7, v7, v198, s[10:11]
	v_cndmask_b32_e64 v8, v8, v198, s[12:13]
	v_cndmask_b32_e64 v9, v9, v198, s[14:15]
	v_cndmask_b32_e64 v10, v10, v198, s[16:17]
	v_cndmask_b32_e64 v11, v11, v198, s[18:19]
	v_cndmask_b32_e64 v12, v12, v198, s[20:21]
	v_cndmask_b32_e64 v13, v13, v198, s[22:23]
	v_cndmask_b32_e64 v14, v14, v198, s[24:25]
	v_cndmask_b32_e64 v15, v15, v198, s[26:27]
	v_cndmask_b32_e64 v16, v16, v198, s[28:29]
	v_cndmask_b32_e64 v17, v17, v198, s[30:31]
.Lq2_nd0_0:
	v_mfma_scale_f32_32x32x64_f8f6f4 v[18:33], v[66:73], v[106:113], 0, v203, v203 op_sel_hi:[0,0,0]
	v_exp_f32_e64 v2, -v2
	v_exp_f32_e64 v3, -v3
	v_exp_f32_e64 v4, -v4
	v_exp_f32_e64 v5, -v5
	s_waitcnt lgkmcnt(0)
	v_add_co_u32_e64 v200, s[42:43], v200, v200
	v_add_co_u32_e64 v200, s[48:49], v200, v200
	v_add_co_u32_e64 v200, s[50:51], v200, v200
	v_add_co_u32_e64 v200, s[56:57], v200, v200
	v_add_f32_e32 v2, v2, v162
	v_add_f32_e32 v3, v3, v163
	v_add_f32_e32 v4, v4, v164
	v_add_f32_e32 v5, v5, v165
	v_cndmask_b32_e64 v204, 1.0, v2, s[42:43]
	v_cndmask_b32_e64 v205, 1.0, v3, s[48:49]
	v_cndmask_b32_e64 v206, 1.0, v4, s[50:51]
	v_cndmask_b32_e64 v207, 1.0, v5, s[56:57]
	v_mfma_scale_f32_32x32x64_f8f6f4 v[18:33], v[74:81], v[122:129], v[18:33], v203, v203 op_sel_hi:[0,0,0]
	v_exp_f32_e64 v6, -v6
	v_exp_f32_e64 v7, -v7
	v_exp_f32_e64 v8, -v8
	v_exp_f32_e64 v9, -v9
	v_add_co_u32_e64 v200, s[42:43], v200, v200
	v_add_co_u32_e64 v200, s[48:49], v200, v200
	v_add_co_u32_e64 v200, s[50:51], v200, v200
	v_add_co_u32_e64 v200, s[56:57], v200, v200
	v_add_f32_e32 v6, v6, v166
	v_add_f32_e32 v7, v7, v167
	v_add_f32_e32 v8, v8, v168
	v_add_f32_e32 v9, v9, v169
	v_cndmask_b32_e64 v208, 1.0, v6, s[42:43]
	v_cndmask_b32_e64 v209, 1.0, v7, s[48:49]
	v_cndmask_b32_e64 v210, 1.0, v8, s[50:51]
	v_cndmask_b32_e64 v211, 1.0, v9, s[56:57]
	v_mfma_scale_f32_32x32x64_f8f6f4 v[18:33], v[82:89], v[114:121], v[18:33], v203, v203 op_sel_hi:[0,0,0]
	v_exp_f32_e64 v10, -v10
	v_exp_f32_e64 v11, -v11
	v_exp_f32_e64 v12, -v12
	v_exp_f32_e64 v13, -v13
	v_add_co_u32_e64 v200, s[42:43], v200, v200
	v_add_co_u32_e64 v200, s[48:49], v200, v200
	v_add_co_u32_e64 v200, s[50:51], v200, v200
	v_add_co_u32_e64 v200, s[56:57], v200, v200
	v_add_f32_e32 v10, v10, v170
	v_add_f32_e32 v11, v11, v171
	v_add_f32_e32 v12, v12, v172
	v_add_f32_e32 v13, v13, v173
	v_cndmask_b32_e64 v212, 1.0, v10, s[42:43]
	v_cndmask_b32_e64 v213, 1.0, v11, s[48:49]
	v_cndmask_b32_e64 v214, 1.0, v12, s[50:51]
	v_cndmask_b32_e64 v215, 1.0, v13, s[56:57]
	v_mfma_scale_f32_32x32x64_f8f6f4 v[18:33], v[90:97], v[98:105], v[18:33], v203, v203 op_sel_hi:[0,0,0]
	s_add_i32 s34, s54, 1
	s_and_b32 s34, s34, 15
	s_lshl_b32 s34, s34, 3
	s_add_i32 s34, s34, s52
	s_lshl_b32 s34, s34, 13
	s_add_i32 s34, s34, s53
	buffer_load_dwordx4 v[106:109], v195, s[44:47], s34 offen
	s_or_b32 s42, s34, 0x400
	buffer_load_dwordx4 v[110:113], v195, s[44:47], s42 offen
	s_or_b32 s43, s34, 0x800
	buffer_load_dwordx4 v[122:125], v195, s[44:47], s43 offen
	s_or_b32 s42, s34, 0xc00
	buffer_load_dwordx4 v[126:129], v195, s[44:47], s42 offen
	s_or_b32 s43, s34, 0x1000
	buffer_load_dwordx4 v[114:117], v195, s[44:47], s43 offen
	s_or_b32 s42, s34, 0x1400
	buffer_load_dwordx4 v[118:121], v195, s[44:47], s42 offen
	s_or_b32 s43, s34, 0x1800
	buffer_load_dwordx4 v[98:101], v195, s[44:47], s43 offen
	s_or_b32 s42, s34, 0x1c00
	buffer_load_dwordx4 v[102:105], v195, s[44:47], s42 offen
	v_exp_f32_e64 v14, -v14
	v_exp_f32_e64 v15, -v15
	v_exp_f32_e64 v16, -v16
	v_exp_f32_e64 v17, -v17
	v_add_co_u32_e64 v200, s[42:43], v200, v200
	v_add_co_u32_e64 v200, s[48:49], v200, v200
	v_add_co_u32_e64 v200, s[50:51], v200, v200
	v_add_co_u32_e64 v200, s[56:57], v200, v200
	v_add_f32_e32 v14, v14, v174
	v_add_f32_e32 v15, v15, v175
	v_add_f32_e32 v16, v16, v176
	v_add_f32_e32 v17, v17, v177
	v_cndmask_b32_e64 v216, 1.0, v14, s[42:43]
	v_cndmask_b32_e64 v217, 1.0, v15, s[48:49]
	v_cndmask_b32_e64 v218, 1.0, v16, s[50:51]
	v_cndmask_b32_e64 v219, 1.0, v17, s[56:57]
	s_cmp_lg_u32 s55, s40
	s_cbranch_scc1 .Lq2_nd1_0
	s_nop 15
	s_nop 7
	v_cndmask_b32_e64 v18, v18, v199, s[0:1]
	v_cndmask_b32_e64 v19, v19, v199, s[2:3]
	v_cndmask_b32_e64 v20, v20, v199, s[4:5]
	v_cndmask_b32_e64 v21, v21, v199, s[6:7]
	v_cndmask_b32_e64 v22, v22, v199, s[8:9]
	v_cndmask_b32_e64 v23, v23, v199, s[10:11]
	v_cndmask_b32_e64 v24, v24, v199, s[12:13]
	v_cndmask_b32_e64 v25, v25, v199, s[14:15]
	v_cndmask_b32_e64 v26, v26, v199, s[16:17]
	v_cndmask_b32_e64 v27, v27, v199, s[18:19]
	v_cndmask_b32_e64 v28, v28, v199, s[20:21]
	v_cndmask_b32_e64 v29, v29, v199, s[22:23]
	v_cndmask_b32_e64 v30, v30, v199, s[24:25]
	v_cndmask_b32_e64 v31, v31, v199, s[26:27]
	v_cndmask_b32_e64 v32, v32, v199, s[28:29]
	v_cndmask_b32_e64 v33, v33, v199, s[30:31]
.Lq2_nd1_0:
	s_nop 3
	s_waitcnt vmcnt(14)
	v_mfma_scale_f32_32x32x64_f8f6f4 v[2:17], v[34:41], v[146:153], 0, v203, v203 op_sel_hi:[0,0,0]
	v_exp_f32_e64 v18, -v18
	v_exp_f32_e64 v19, -v19
	v_exp_f32_e64 v20, -v20
	v_exp_f32_e64 v21, -v21
	v_add_co_u32_e64 v200, s[42:43], v200, v200
	v_add_co_u32_e64 v200, s[48:49], v200, v200
	v_add_co_u32_e64 v200, s[50:51], v200, v200
	v_add_co_u32_e64 v200, s[56:57], v200, v200
	v_add_f32_e32 v18, v18, v178
	v_add_f32_e32 v19, v19, v179
	v_add_f32_e32 v20, v20, v180
	v_add_f32_e32 v21, v21, v181
	v_cndmask_b32_e64 v220, 1.0, v18, s[42:43]
	v_cndmask_b32_e64 v221, 1.0, v19, s[48:49]
	v_cndmask_b32_e64 v222, 1.0, v20, s[50:51]
	v_cndmask_b32_e64 v223, 1.0, v21, s[56:57]
	s_waitcnt vmcnt(12)
	v_mfma_scale_f32_32x32x64_f8f6f4 v[2:17], v[42:49], v[154:161], v[2:17], v203, v203 op_sel_hi:[0,0,0]
	v_exp_f32_e64 v22, -v22
	v_exp_f32_e64 v23, -v23
	v_exp_f32_e64 v24, -v24
	v_exp_f32_e64 v25, -v25
	v_add_co_u32_e64 v200, s[42:43], v200, v200
	v_add_co_u32_e64 v200, s[48:49], v200, v200
	v_add_co_u32_e64 v200, s[50:51], v200, v200
	v_add_co_u32_e64 v200, s[56:57], v200, v200
	v_add_f32_e32 v22, v22, v182
	v_add_f32_e32 v23, v23, v183
	v_add_f32_e32 v24, v24, v184
	v_add_f32_e32 v25, v25, v185
	v_cndmask_b32_e64 v224, 1.0, v22, s[42:43]
	v_cndmask_b32_e64 v225, 1.0, v23, s[48:49]
	v_cndmask_b32_e64 v226, 1.0, v24, s[50:51]
	v_cndmask_b32_e64 v227, 1.0, v25, s[56:57]
	s_waitcnt vmcnt(10)
	v_mfma_scale_f32_32x32x64_f8f6f4 v[2:17], v[50:57], v[138:145], v[2:17], v203, v203 op_sel_hi:[0,0,0]
	v_exp_f32_e64 v26, -v26
	v_exp_f32_e64 v27, -v27
	v_exp_f32_e64 v28, -v28
	v_exp_f32_e64 v29, -v29
	v_add_co_u32_e64 v200, s[42:43], v200, v200
	v_add_co_u32_e64 v200, s[48:49], v200, v200
	v_add_co_u32_e64 v200, s[50:51], v200, v200
	v_add_co_u32_e64 v200, s[56:57], v200, v200
	v_add_f32_e32 v26, v26, v186
	v_add_f32_e32 v27, v27, v187
	v_add_f32_e32 v28, v28, v188
	v_add_f32_e32 v29, v29, v189
	v_cndmask_b32_e64 v228, 1.0, v26, s[42:43]
	v_cndmask_b32_e64 v229, 1.0, v27, s[48:49]
	v_cndmask_b32_e64 v230, 1.0, v28, s[50:51]
	v_cndmask_b32_e64 v231, 1.0, v29, s[56:57]
	s_waitcnt vmcnt(8)
	v_mfma_scale_f32_32x32x64_f8f6f4 v[2:17], v[58:65], v[130:137], v[2:17], v203, v203 op_sel_hi:[0,0,0]
	v_exp_f32_e64 v30, -v30
	v_exp_f32_e64 v31, -v31
	v_exp_f32_e64 v32, -v32
	v_exp_f32_e64 v33, -v33
	v_add_co_u32_e64 v200, s[42:43], v200, v200
	v_add_co_u32_e64 v200, s[48:49], v200, v200
	v_add_co_u32_e64 v200, s[50:51], v200, v200
	v_add_co_u32_e64 v200, s[56:57], v200, v200
	v_add_f32_e32 v30, v30, v190
	v_add_f32_e32 v31, v31, v191
	v_add_f32_e32 v32, v32, v192
	v_add_f32_e32 v33, v33, v193
	v_cndmask_b32_e64 v232, 1.0, v30, s[42:43]
	v_cndmask_b32_e64 v233, 1.0, v31, s[48:49]
	v_cndmask_b32_e64 v234, 1.0, v32, s[50:51]
	v_cndmask_b32_e64 v235, 1.0, v33, s[56:57]
	s_lshl_b32 s34, s39, 2
	s_add_i32 s34, s34, 1
	s_add_i32 s34, s34, s35
	s_and_b32 s41, s34, 15
	s_add_i32 s54, s34, 1
	s_and_b32 s54, s54, 15
	s_lshl_b32 s55, s41, 8
	s_lshl_b32 s38, s52, 12
	s_add_i32 s55, s55, s38
	v_lshl_add_u32 v236, v194, 2, s55
	ds_read_b32 v200, v236
	s_lshl_b32 s55, s41, 3
	s_add_i32 s55, s55, s52
	s_cmp_lg_u32 s55, s33
	s_cbranch_scc1 .Lq2_nd0_1
	v_cndmask_b32_e64 v2, v2, v198, s[0:1]
	v_cndmask_b32_e64 v3, v3, v198, s[2:3]
	v_cndmask_b32_e64 v4, v4, v198, s[4:5]
	v_cndmask_b32_e64 v5, v5, v198, s[6:7]
	v_cndmask_b32_e64 v6, v6, v198, s[8:9]
	v_cndmask_b32_e64 v7, v7, v198, s[10:11]
	v_cndmask_b32_e64 v8, v8, v198, s[12:13]
	v_cndmask_b32_e64 v9, v9, v198, s[14:15]
	v_cndmask_b32_e64 v10, v10, v198, s[16:17]
	v_cndmask_b32_e64 v11, v11, v198, s[18:19]
	v_cndmask_b32_e64 v12, v12, v198, s[20:21]
	v_cndmask_b32_e64 v13, v13, v198, s[22:23]
	v_cndmask_b32_e64 v14, v14, v198, s[24:25]
	v_cndmask_b32_e64 v15, v15, v198, s[26:27]
	v_cndmask_b32_e64 v16, v16, v198, s[28:29]
	v_cndmask_b32_e64 v17, v17, v198, s[30:31]
.Lq2_nd0_1:
	v_mfma_scale_f32_32x32x64_f8f6f4 v[18:33], v[66:73], v[146:153], 0, v203, v203 op_sel_hi:[0,0,0]
	v_exp_f32_e64 v2, -v2
	v_exp_f32_e64 v3, -v3
	v_exp_f32_e64 v4, -v4
	v_exp_f32_e64 v5, -v5
	s_waitcnt lgkmcnt(0)
	v_add_co_u32_e64 v200, s[42:43], v200, v200
	v_add_co_u32_e64 v200, s[48:49], v200, v200
	v_add_co_u32_e64 v200, s[50:51], v200, v200
	v_add_co_u32_e64 v200, s[56:57], v200, v200
	v_add_f32_e32 v2, v2, v162
	v_add_f32_e32 v3, v3, v163
	v_add_f32_e32 v4, v4, v164
	v_add_f32_e32 v5, v5, v165
	v_cndmask_b32_e64 v2, 1.0, v2, s[42:43]
	v_cndmask_b32_e64 v3, 1.0, v3, s[48:49]
	v_cndmask_b32_e64 v4, 1.0, v4, s[50:51]
	v_cndmask_b32_e64 v5, 1.0, v5, s[56:57]
	v_mul_f32_e32 v204, v204, v2
	v_mul_f32_e32 v205, v205, v3
	v_mul_f32_e32 v206, v206, v4
	v_mul_f32_e32 v207, v207, v5
	v_mfma_scale_f32_32x32x64_f8f6f4 v[18:33], v[74:81], v[154:161], v[18:33], v203, v203 op_sel_hi:[0,0,0]
	v_exp_f32_e64 v6, -v6
	v_exp_f32_e64 v7, -v7
	v_exp_f32_e64 v8, -v8
	v_exp_f32_e64 v9, -v9
	v_add_co_u32_e64 v200, s[42:43], v200, v200
	v_add_co_u32_e64 v200, s[48:49], v200, v200
	v_add_co_u32_e64 v200, s[50:51], v200, v200
	v_add_co_u32_e64 v200, s[56:57], v200, v200
	v_add_f32_e32 v6, v6, v166
	v_add_f32_e32 v7, v7, v167
	v_add_f32_e32 v8, v8, v168
	v_add_f32_e32 v9, v9, v169
	v_cndmask_b32_e64 v6, 1.0, v6, s[42:43]
	v_cndmask_b32_e64 v7, 1.0, v7, s[48:49]
	v_cndmask_b32_e64 v8, 1.0, v8, s[50:51]
	v_cndmask_b32_e64 v9, 1.0, v9, s[56:57]
	v_mul_f32_e32 v208, v208, v6
	v_mul_f32_e32 v209, v209, v7
	v_mul_f32_e32 v210, v210, v8
	v_mul_f32_e32 v211, v211, v9
	v_mfma_scale_f32_32x32x64_f8f6f4 v[18:33], v[82:89], v[138:145], v[18:33], v203, v203 op_sel_hi:[0,0,0]
	v_exp_f32_e64 v10, -v10
	v_exp_f32_e64 v11, -v11
	v_exp_f32_e64 v12, -v12
	v_exp_f32_e64 v13, -v13
	v_add_co_u32_e64 v200, s[42:43], v200, v200
	v_add_co_u32_e64 v200, s[48:49], v200, v200
	v_add_co_u32_e64 v200, s[50:51], v200, v200
	v_add_co_u32_e64 v200, s[56:57], v200, v200
	v_add_f32_e32 v10, v10, v170
	v_add_f32_e32 v11, v11, v171
	v_add_f32_e32 v12, v12, v172
	v_add_f32_e32 v13, v13, v173
	v_cndmask_b32_e64 v10, 1.0, v10, s[42:43]
	v_cndmask_b32_e64 v11, 1.0, v11, s[48:49]
	v_cndmask_b32_e64 v12, 1.0, v12, s[50:51]
	v_cndmask_b32_e64 v13, 1.0, v13, s[56:57]
	v_mul_f32_e32 v212, v212, v10
	v_mul_f32_e32 v213, v213, v11
	v_mul_f32_e32 v214, v214, v12
	v_mul_f32_e32 v215, v215, v13
	v_mfma_scale_f32_32x32x64_f8f6f4 v[18:33], v[90:97], v[130:137], v[18:33], v203, v203 op_sel_hi:[0,0,0]
	s_add_i32 s34, s54, 1
	s_and_b32 s34, s34, 15
	s_lshl_b32 s34, s34, 3
	s_add_i32 s34, s34, s52
	s_lshl_b32 s34, s34, 13
	s_add_i32 s34, s34, s53
	buffer_load_dwordx4 v[146:149], v195, s[44:47], s34 offen
	s_or_b32 s42, s34, 0x400
	buffer_load_dwordx4 v[150:153], v195, s[44:47], s42 offen
	s_or_b32 s43, s34, 0x800
	buffer_load_dwordx4 v[154:157], v195, s[44:47], s43 offen
	s_or_b32 s42, s34, 0xc00
	buffer_load_dwordx4 v[158:161], v195, s[44:47], s42 offen
	s_or_b32 s43, s34, 0x1000
	buffer_load_dwordx4 v[138:141], v195, s[44:47], s43 offen
	s_or_b32 s42, s34, 0x1400
	buffer_load_dwordx4 v[142:145], v195, s[44:47], s42 offen
	s_or_b32 s43, s34, 0x1800
	buffer_load_dwordx4 v[130:133], v195, s[44:47], s43 offen
	s_or_b32 s42, s34, 0x1c00
	buffer_load_dwordx4 v[134:137], v195, s[44:47], s42 offen
	v_exp_f32_e64 v14, -v14
	v_exp_f32_e64 v15, -v15
	v_exp_f32_e64 v16, -v16
	v_exp_f32_e64 v17, -v17
	v_add_co_u32_e64 v200, s[42:43], v200, v200
	v_add_co_u32_e64 v200, s[48:49], v200, v200
	v_add_co_u32_e64 v200, s[50:51], v200, v200
	v_add_co_u32_e64 v200, s[56:57], v200, v200
	v_add_f32_e32 v14, v14, v174
	v_add_f32_e32 v15, v15, v175
	v_add_f32_e32 v16, v16, v176
	v_add_f32_e32 v17, v17, v177
	v_cndmask_b32_e64 v14, 1.0, v14, s[42:43]
	v_cndmask_b32_e64 v15, 1.0, v15, s[48:49]
	v_cndmask_b32_e64 v16, 1.0, v16, s[50:51]
	v_cndmask_b32_e64 v17, 1.0, v17, s[56:57]
	v_mul_f32_e32 v216, v216, v14
	v_mul_f32_e32 v217, v217, v15
	v_mul_f32_e32 v218, v218, v16
	v_mul_f32_e32 v219, v219, v17
	s_cmp_lg_u32 s55, s40
	s_cbranch_scc1 .Lq2_nd1_1
	s_nop 15
	s_nop 7
	v_cndmask_b32_e64 v18, v18, v199, s[0:1]
	v_cndmask_b32_e64 v19, v19, v199, s[2:3]
	v_cndmask_b32_e64 v20, v20, v199, s[4:5]
	v_cndmask_b32_e64 v21, v21, v199, s[6:7]
	v_cndmask_b32_e64 v22, v22, v199, s[8:9]
	v_cndmask_b32_e64 v23, v23, v199, s[10:11]
	v_cndmask_b32_e64 v24, v24, v199, s[12:13]
	v_cndmask_b32_e64 v25, v25, v199, s[14:15]
	v_cndmask_b32_e64 v26, v26, v199, s[16:17]
	v_cndmask_b32_e64 v27, v27, v199, s[18:19]
	v_cndmask_b32_e64 v28, v28, v199, s[20:21]
	v_cndmask_b32_e64 v29, v29, v199, s[22:23]
	v_cndmask_b32_e64 v30, v30, v199, s[24:25]
	v_cndmask_b32_e64 v31, v31, v199, s[26:27]
	v_cndmask_b32_e64 v32, v32, v199, s[28:29]
	v_cndmask_b32_e64 v33, v33, v199, s[30:31]
.Lq2_nd1_1:
	s_nop 3
	s_waitcnt vmcnt(14)
	v_mfma_scale_f32_32x32x64_f8f6f4 v[2:17], v[34:41], v[106:113], 0, v203, v203 op_sel_hi:[0,0,0]
	v_exp_f32_e64 v18, -v18
	v_exp_f32_e64 v19, -v19
	v_exp_f32_e64 v20, -v20
	v_exp_f32_e64 v21, -v21
	v_add_co_u32_e64 v200, s[42:43], v200, v200
	v_add_co_u32_e64 v200, s[48:49], v200, v200
	v_add_co_u32_e64 v200, s[50:51], v200, v200
	v_add_co_u32_e64 v200, s[56:57], v200, v200
	v_add_f32_e32 v18, v18, v178
	v_add_f32_e32 v19, v19, v179
	v_add_f32_e32 v20, v20, v180
	v_add_f32_e32 v21, v21, v181
	v_cndmask_b32_e64 v18, 1.0, v18, s[42:43]
	v_cndmask_b32_e64 v19, 1.0, v19, s[48:49]
	v_cndmask_b32_e64 v20, 1.0, v20, s[50:51]
	v_cndmask_b32_e64 v21, 1.0, v21, s[56:57]
	v_mul_f32_e32 v220, v220, v18
	v_mul_f32_e32 v221, v221, v19
	v_mul_f32_e32 v222, v222, v20
	v_mul_f32_e32 v223, v223, v21
	s_waitcnt vmcnt(12)
	v_mfma_scale_f32_32x32x64_f8f6f4 v[2:17], v[42:49], v[122:129], v[2:17], v203, v203 op_sel_hi:[0,0,0]
	v_exp_f32_e64 v22, -v22
	v_exp_f32_e64 v23, -v23
	v_exp_f32_e64 v24, -v24
	v_exp_f32_e64 v25, -v25
	v_add_co_u32_e64 v200, s[42:43], v200, v200
	v_add_co_u32_e64 v200, s[48:49], v200, v200
	v_add_co_u32_e64 v200, s[50:51], v200, v200
	v_add_co_u32_e64 v200, s[56:57], v200, v200
	v_add_f32_e32 v22, v22, v182
	v_add_f32_e32 v23, v23, v183
	v_add_f32_e32 v24, v24, v184
	v_add_f32_e32 v25, v25, v185
	v_cndmask_b32_e64 v22, 1.0, v22, s[42:43]
	v_cndmask_b32_e64 v23, 1.0, v23, s[48:49]
	v_cndmask_b32_e64 v24, 1.0, v24, s[50:51]
	v_cndmask_b32_e64 v25, 1.0, v25, s[56:57]
	v_mul_f32_e32 v224, v224, v22
	v_mul_f32_e32 v225, v225, v23
	v_mul_f32_e32 v226, v226, v24
	v_mul_f32_e32 v227, v227, v25
	s_waitcnt vmcnt(10)
	v_mfma_scale_f32_32x32x64_f8f6f4 v[2:17], v[50:57], v[114:121], v[2:17], v203, v203 op_sel_hi:[0,0,0]
	v_exp_f32_e64 v26, -v26
	v_exp_f32_e64 v27, -v27
	v_exp_f32_e64 v28, -v28
	v_exp_f32_e64 v29, -v29
	v_add_co_u32_e64 v200, s[42:43], v200, v200
	v_add_co_u32_e64 v200, s[48:49], v200, v200
	v_add_co_u32_e64 v200, s[50:51], v200, v200
	v_add_co_u32_e64 v200, s[56:57], v200, v200
	v_add_f32_e32 v26, v26, v186
	v_add_f32_e32 v27, v27, v187
	v_add_f32_e32 v28, v28, v188
	v_add_f32_e32 v29, v29, v189
	v_cndmask_b32_e64 v26, 1.0, v26, s[42:43]
	v_cndmask_b32_e64 v27, 1.0, v27, s[48:49]
	v_cndmask_b32_e64 v28, 1.0, v28, s[50:51]
	v_cndmask_b32_e64 v29, 1.0, v29, s[56:57]
	v_mul_f32_e32 v228, v228, v26
	v_mul_f32_e32 v229, v229, v27
	v_mul_f32_e32 v230, v230, v28
	v_mul_f32_e32 v231, v231, v29
	s_waitcnt vmcnt(8)
	v_mfma_scale_f32_32x32x64_f8f6f4 v[2:17], v[58:65], v[98:105], v[2:17], v203, v203 op_sel_hi:[0,0,0]
	v_exp_f32_e64 v30, -v30
	v_exp_f32_e64 v31, -v31
	v_exp_f32_e64 v32, -v32
	v_exp_f32_e64 v33, -v33
	v_add_co_u32_e64 v200, s[42:43], v200, v200
	v_add_co_u32_e64 v200, s[48:49], v200, v200
	v_add_co_u32_e64 v200, s[50:51], v200, v200
	v_add_co_u32_e64 v200, s[56:57], v200, v200
	v_add_f32_e32 v30, v30, v190
	v_add_f32_e32 v31, v31, v191
	v_add_f32_e32 v32, v32, v192
	v_add_f32_e32 v33, v33, v193
	v_cndmask_b32_e64 v30, 1.0, v30, s[42:43]
	v_cndmask_b32_e64 v31, 1.0, v31, s[48:49]
	v_cndmask_b32_e64 v32, 1.0, v32, s[50:51]
	v_cndmask_b32_e64 v33, 1.0, v33, s[56:57]
	v_mul_f32_e32 v232, v232, v30
	v_mul_f32_e32 v233, v233, v31
	v_mul_f32_e32 v234, v234, v32
	v_mul_f32_e32 v235, v235, v33
	s_lshl_b32 s34, s39, 2
	s_add_i32 s34, s34, 2
	s_add_i32 s34, s34, s35
	s_and_b32 s41, s34, 15
	s_add_i32 s54, s34, 1
	s_and_b32 s54, s54, 15
	s_lshl_b32 s55, s41, 8
	s_lshl_b32 s38, s52, 12
	s_add_i32 s55, s55, s38
	v_lshl_add_u32 v236, v194, 2, s55
	ds_read_b32 v200, v236
	s_lshl_b32 s55, s41, 3
	s_add_i32 s55, s55, s52
	s_cmp_lg_u32 s55, s33
	s_cbranch_scc1 .Lq2_nd0_2
	v_cndmask_b32_e64 v2, v2, v198, s[0:1]
	v_cndmask_b32_e64 v3, v3, v198, s[2:3]
	v_cndmask_b32_e64 v4, v4, v198, s[4:5]
	v_cndmask_b32_e64 v5, v5, v198, s[6:7]
	v_cndmask_b32_e64 v6, v6, v198, s[8:9]
	v_cndmask_b32_e64 v7, v7, v198, s[10:11]
	v_cndmask_b32_e64 v8, v8, v198, s[12:13]
	v_cndmask_b32_e64 v9, v9, v198, s[14:15]
	v_cndmask_b32_e64 v10, v10, v198, s[16:17]
	v_cndmask_b32_e64 v11, v11, v198, s[18:19]
	v_cndmask_b32_e64 v12, v12, v198, s[20:21]
	v_cndmask_b32_e64 v13, v13, v198, s[22:23]
	v_cndmask_b32_e64 v14, v14, v198, s[24:25]
	v_cndmask_b32_e64 v15, v15, v198, s[26:27]
	v_cndmask_b32_e64 v16, v16, v198, s[28:29]
	v_cndmask_b32_e64 v17, v17, v198, s[30:31]
.Lq2_nd0_2:
	v_mfma_scale_f32_32x32x64_f8f6f4 v[18:33], v[66:73], v[106:113], 0, v203, v203 op_sel_hi:[0,0,0]
	v_exp_f32_e64 v2, -v2
	v_exp_f32_e64 v3, -v3
	v_exp_f32_e64 v4, -v4
	v_exp_f32_e64 v5, -v5
	s_waitcnt lgkmcnt(0)
	v_add_co_u32_e64 v200, s[42:43], v200, v200
	v_add_co_u32_e64 v200, s[48:49], v200, v200
	v_add_co_u32_e64 v200, s[50:51], v200, v200
	v_add_co_u32_e64 v200, s[56:57], v200, v200
	v_add_f32_e32 v2, v2, v162
	v_add_f32_e32 v3, v3, v163
	v_add_f32_e32 v4, v4, v164
	v_add_f32_e32 v5, v5, v165
	v_cndmask_b32_e64 v2, 1.0, v2, s[42:43]
	v_cndmask_b32_e64 v3, 1.0, v3, s[48:49]
	v_cndmask_b32_e64 v4, 1.0, v4, s[50:51]
	v_cndmask_b32_e64 v5, 1.0, v5, s[56:57]
	v_mul_f32_e32 v204, v204, v2
	v_mul_f32_e32 v205, v205, v3
	v_mul_f32_e32 v206, v206, v4
	v_mul_f32_e32 v207, v207, v5
	v_mfma_scale_f32_32x32x64_f8f6f4 v[18:33], v[74:81], v[122:129], v[18:33], v203, v203 op_sel_hi:[0,0,0]
	v_exp_f32_e64 v6, -v6
	v_exp_f32_e64 v7, -v7
	v_exp_f32_e64 v8, -v8
	v_exp_f32_e64 v9, -v9
	v_add_co_u32_e64 v200, s[42:43], v200, v200
	v_add_co_u32_e64 v200, s[48:49], v200, v200
	v_add_co_u32_e64 v200, s[50:51], v200, v200
	v_add_co_u32_e64 v200, s[56:57], v200, v200
	v_add_f32_e32 v6, v6, v166
	v_add_f32_e32 v7, v7, v167
	v_add_f32_e32 v8, v8, v168
	v_add_f32_e32 v9, v9, v169
	v_cndmask_b32_e64 v6, 1.0, v6, s[42:43]
	v_cndmask_b32_e64 v7, 1.0, v7, s[48:49]
	v_cndmask_b32_e64 v8, 1.0, v8, s[50:51]
	v_cndmask_b32_e64 v9, 1.0, v9, s[56:57]
	v_mul_f32_e32 v208, v208, v6
	v_mul_f32_e32 v209, v209, v7
	v_mul_f32_e32 v210, v210, v8
	v_mul_f32_e32 v211, v211, v9
	v_mfma_scale_f32_32x32x64_f8f6f4 v[18:33], v[82:89], v[114:121], v[18:33], v203, v203 op_sel_hi:[0,0,0]
	v_exp_f32_e64 v10, -v10
	v_exp_f32_e64 v11, -v11
	v_exp_f32_e64 v12, -v12
	v_exp_f32_e64 v13, -v13
	v_add_co_u32_e64 v200, s[42:43], v200, v200
	v_add_co_u32_e64 v200, s[48:49], v200, v200
	v_add_co_u32_e64 v200, s[50:51], v200, v200
	v_add_co_u32_e64 v200, s[56:57], v200, v200
	v_add_f32_e32 v10, v10, v170
	v_add_f32_e32 v11, v11, v171
	v_add_f32_e32 v12, v12, v172
	v_add_f32_e32 v13, v13, v173
	v_cndmask_b32_e64 v10, 1.0, v10, s[42:43]
	v_cndmask_b32_e64 v11, 1.0, v11, s[48:49]
	v_cndmask_b32_e64 v12, 1.0, v12, s[50:51]
	v_cndmask_b32_e64 v13, 1.0, v13, s[56:57]
	v_mul_f32_e32 v212, v212, v10
	v_mul_f32_e32 v213, v213, v11
	v_mul_f32_e32 v214, v214, v12
	v_mul_f32_e32 v215, v215, v13
	v_mfma_scale_f32_32x32x64_f8f6f4 v[18:33], v[90:97], v[98:105], v[18:33], v203, v203 op_sel_hi:[0,0,0]
	s_add_i32 s34, s54, 1
	s_and_b32 s34, s34, 15
	s_lshl_b32 s34, s34, 3
	s_add_i32 s34, s34, s52
	s_lshl_b32 s34, s34, 13
	s_add_i32 s34, s34, s53
	buffer_load_dwordx4 v[106:109], v195, s[44:47], s34 offen
	s_or_b32 s42, s34, 0x400
	buffer_load_dwordx4 v[110:113], v195, s[44:47], s42 offen
	s_or_b32 s43, s34, 0x800
	buffer_load_dwordx4 v[122:125], v195, s[44:47], s43 offen
	s_or_b32 s42, s34, 0xc00
	buffer_load_dwordx4 v[126:129], v195, s[44:47], s42 offen
	s_or_b32 s43, s34, 0x1000
	buffer_load_dwordx4 v[114:117], v195, s[44:47], s43 offen
	s_or_b32 s42, s34, 0x1400
	buffer_load_dwordx4 v[118:121], v195, s[44:47], s42 offen
	s_or_b32 s43, s34, 0x1800
	buffer_load_dwordx4 v[98:101], v195, s[44:47], s43 offen
	s_or_b32 s42, s34, 0x1c00
	buffer_load_dwordx4 v[102:105], v195, s[44:47], s42 offen
	v_exp_f32_e64 v14, -v14
	v_exp_f32_e64 v15, -v15
	v_exp_f32_e64 v16, -v16
	v_exp_f32_e64 v17, -v17
	v_add_co_u32_e64 v200, s[42:43], v200, v200
	v_add_co_u32_e64 v200, s[48:49], v200, v200
	v_add_co_u32_e64 v200, s[50:51], v200, v200
	v_add_co_u32_e64 v200, s[56:57], v200, v200
	v_add_f32_e32 v14, v14, v174
	v_add_f32_e32 v15, v15, v175
	v_add_f32_e32 v16, v16, v176
	v_add_f32_e32 v17, v17, v177
	v_cndmask_b32_e64 v14, 1.0, v14, s[42:43]
	v_cndmask_b32_e64 v15, 1.0, v15, s[48:49]
	v_cndmask_b32_e64 v16, 1.0, v16, s[50:51]
	v_cndmask_b32_e64 v17, 1.0, v17, s[56:57]
	v_mul_f32_e32 v216, v216, v14
	v_mul_f32_e32 v217, v217, v15
	v_mul_f32_e32 v218, v218, v16
	v_mul_f32_e32 v219, v219, v17
	s_cmp_lg_u32 s55, s40
	s_cbranch_scc1 .Lq2_nd1_2
	s_nop 15
	s_nop 7
	v_cndmask_b32_e64 v18, v18, v199, s[0:1]
	v_cndmask_b32_e64 v19, v19, v199, s[2:3]
	v_cndmask_b32_e64 v20, v20, v199, s[4:5]
	v_cndmask_b32_e64 v21, v21, v199, s[6:7]
	v_cndmask_b32_e64 v22, v22, v199, s[8:9]
	v_cndmask_b32_e64 v23, v23, v199, s[10:11]
	v_cndmask_b32_e64 v24, v24, v199, s[12:13]
	v_cndmask_b32_e64 v25, v25, v199, s[14:15]
	v_cndmask_b32_e64 v26, v26, v199, s[16:17]
	v_cndmask_b32_e64 v27, v27, v199, s[18:19]
	v_cndmask_b32_e64 v28, v28, v199, s[20:21]
	v_cndmask_b32_e64 v29, v29, v199, s[22:23]
	v_cndmask_b32_e64 v30, v30, v199, s[24:25]
	v_cndmask_b32_e64 v31, v31, v199, s[26:27]
	v_cndmask_b32_e64 v32, v32, v199, s[28:29]
	v_cndmask_b32_e64 v33, v33, v199, s[30:31]
.Lq2_nd1_2:
	s_nop 3
	s_waitcnt vmcnt(14)
	v_mfma_scale_f32_32x32x64_f8f6f4 v[2:17], v[34:41], v[146:153], 0, v203, v203 op_sel_hi:[0,0,0]
	v_exp_f32_e64 v18, -v18
	v_exp_f32_e64 v19, -v19
	v_exp_f32_e64 v20, -v20
	v_exp_f32_e64 v21, -v21
	v_add_co_u32_e64 v200, s[42:43], v200, v200
	v_add_co_u32_e64 v200, s[48:49], v200, v200
	v_add_co_u32_e64 v200, s[50:51], v200, v200
	v_add_co_u32_e64 v200, s[56:57], v200, v200
	v_add_f32_e32 v18, v18, v178
	v_add_f32_e32 v19, v19, v179
	v_add_f32_e32 v20, v20, v180
	v_add_f32_e32 v21, v21, v181
	v_cndmask_b32_e64 v18, 1.0, v18, s[42:43]
	v_cndmask_b32_e64 v19, 1.0, v19, s[48:49]
	v_cndmask_b32_e64 v20, 1.0, v20, s[50:51]
	v_cndmask_b32_e64 v21, 1.0, v21, s[56:57]
	v_mul_f32_e32 v220, v220, v18
	v_mul_f32_e32 v221, v221, v19
	v_mul_f32_e32 v222, v222, v20
	v_mul_f32_e32 v223, v223, v21
	s_waitcnt vmcnt(12)
	v_mfma_scale_f32_32x32x64_f8f6f4 v[2:17], v[42:49], v[154:161], v[2:17], v203, v203 op_sel_hi:[0,0,0]
	v_exp_f32_e64 v22, -v22
	v_exp_f32_e64 v23, -v23
	v_exp_f32_e64 v24, -v24
	v_exp_f32_e64 v25, -v25
	v_add_co_u32_e64 v200, s[42:43], v200, v200
	v_add_co_u32_e64 v200, s[48:49], v200, v200
	v_add_co_u32_e64 v200, s[50:51], v200, v200
	v_add_co_u32_e64 v200, s[56:57], v200, v200
	v_add_f32_e32 v22, v22, v182
	v_add_f32_e32 v23, v23, v183
	v_add_f32_e32 v24, v24, v184
	v_add_f32_e32 v25, v25, v185
	v_cndmask_b32_e64 v22, 1.0, v22, s[42:43]
	v_cndmask_b32_e64 v23, 1.0, v23, s[48:49]
	v_cndmask_b32_e64 v24, 1.0, v24, s[50:51]
	v_cndmask_b32_e64 v25, 1.0, v25, s[56:57]
	v_mul_f32_e32 v224, v224, v22
	v_mul_f32_e32 v225, v225, v23
	v_mul_f32_e32 v226, v226, v24
	v_mul_f32_e32 v227, v227, v25
	s_waitcnt vmcnt(10)
	v_mfma_scale_f32_32x32x64_f8f6f4 v[2:17], v[50:57], v[138:145], v[2:17], v203, v203 op_sel_hi:[0,0,0]
	v_exp_f32_e64 v26, -v26
	v_exp_f32_e64 v27, -v27
	v_exp_f32_e64 v28, -v28
	v_exp_f32_e64 v29, -v29
	v_add_co_u32_e64 v200, s[42:43], v200, v200
	v_add_co_u32_e64 v200, s[48:49], v200, v200
	v_add_co_u32_e64 v200, s[50:51], v200, v200
	v_add_co_u32_e64 v200, s[56:57], v200, v200
	v_add_f32_e32 v26, v26, v186
	v_add_f32_e32 v27, v27, v187
	v_add_f32_e32 v28, v28, v188
	v_add_f32_e32 v29, v29, v189
	v_cndmask_b32_e64 v26, 1.0, v26, s[42:43]
	v_cndmask_b32_e64 v27, 1.0, v27, s[48:49]
	v_cndmask_b32_e64 v28, 1.0, v28, s[50:51]
	v_cndmask_b32_e64 v29, 1.0, v29, s[56:57]
	v_mul_f32_e32 v228, v228, v26
	v_mul_f32_e32 v229, v229, v27
	v_mul_f32_e32 v230, v230, v28
	v_mul_f32_e32 v231, v231, v29
	s_waitcnt vmcnt(8)
	v_mfma_scale_f32_32x32x64_f8f6f4 v[2:17], v[58:65], v[130:137], v[2:17], v203, v203 op_sel_hi:[0,0,0]
	v_exp_f32_e64 v30, -v30
	v_exp_f32_e64 v31, -v31
	v_exp_f32_e64 v32, -v32
	v_exp_f32_e64 v33, -v33
	v_add_co_u32_e64 v200, s[42:43], v200, v200
	v_add_co_u32_e64 v200, s[48:49], v200, v200
	v_add_co_u32_e64 v200, s[50:51], v200, v200
	v_add_co_u32_e64 v200, s[56:57], v200, v200
	v_add_f32_e32 v30, v30, v190
	v_add_f32_e32 v31, v31, v191
	v_add_f32_e32 v32, v32, v192
	v_add_f32_e32 v33, v33, v193
	v_cndmask_b32_e64 v30, 1.0, v30, s[42:43]
	v_cndmask_b32_e64 v31, 1.0, v31, s[48:49]
	v_cndmask_b32_e64 v32, 1.0, v32, s[50:51]
	v_cndmask_b32_e64 v33, 1.0, v33, s[56:57]
	v_mul_f32_e32 v232, v232, v30
	v_mul_f32_e32 v233, v233, v31
	v_mul_f32_e32 v234, v234, v32
	v_mul_f32_e32 v235, v235, v33
	s_lshl_b32 s34, s39, 2
	s_add_i32 s34, s34, 3
	s_add_i32 s34, s34, s35
	s_and_b32 s41, s34, 15
	s_add_i32 s54, s34, 1
	s_and_b32 s54, s54, 15
	s_lshl_b32 s55, s41, 8
	s_lshl_b32 s38, s52, 12
	s_add_i32 s55, s55, s38
	v_lshl_add_u32 v236, v194, 2, s55
	ds_read_b32 v200, v236
	s_lshl_b32 s55, s41, 3
	s_add_i32 s55, s55, s52
	s_cmp_lg_u32 s55, s33
	s_cbranch_scc1 .Lq2_nd0_3
	v_cndmask_b32_e64 v2, v2, v198, s[0:1]
	v_cndmask_b32_e64 v3, v3, v198, s[2:3]
	v_cndmask_b32_e64 v4, v4, v198, s[4:5]
	v_cndmask_b32_e64 v5, v5, v198, s[6:7]
	v_cndmask_b32_e64 v6, v6, v198, s[8:9]
	v_cndmask_b32_e64 v7, v7, v198, s[10:11]
	v_cndmask_b32_e64 v8, v8, v198, s[12:13]
	v_cndmask_b32_e64 v9, v9, v198, s[14:15]
	v_cndmask_b32_e64 v10, v10, v198, s[16:17]
	v_cndmask_b32_e64 v11, v11, v198, s[18:19]
	v_cndmask_b32_e64 v12, v12, v198, s[20:21]
	v_cndmask_b32_e64 v13, v13, v198, s[22:23]
	v_cndmask_b32_e64 v14, v14, v198, s[24:25]
	v_cndmask_b32_e64 v15, v15, v198, s[26:27]
	v_cndmask_b32_e64 v16, v16, v198, s[28:29]
	v_cndmask_b32_e64 v17, v17, v198, s[30:31]
.Lq2_nd0_3:
	v_mfma_scale_f32_32x32x64_f8f6f4 v[18:33], v[66:73], v[146:153], 0, v203, v203 op_sel_hi:[0,0,0]
	ds_read_b128 v[236:239], v202
	v_exp_f32_e64 v2, -v2
	v_exp_f32_e64 v3, -v3
	v_exp_f32_e64 v4, -v4
	v_exp_f32_e64 v5, -v5
	s_waitcnt lgkmcnt(1)
	v_add_co_u32_e64 v200, s[42:43], v200, v200
	v_add_co_u32_e64 v200, s[48:49], v200, v200
	v_add_co_u32_e64 v200, s[50:51], v200, v200
	v_add_co_u32_e64 v200, s[56:57], v200, v200
	v_add_f32_e32 v2, v2, v162
	v_add_f32_e32 v3, v3, v163
	v_add_f32_e32 v4, v4, v164
	v_add_f32_e32 v5, v5, v165
	v_cndmask_b32_e64 v2, 1.0, v2, s[42:43]
	v_cndmask_b32_e64 v3, 1.0, v3, s[48:49]
	v_cndmask_b32_e64 v4, 1.0, v4, s[50:51]
	v_cndmask_b32_e64 v5, 1.0, v5, s[56:57]
	v_mul_f32_e32 v2, v204, v2
	v_mul_f32_e32 v3, v205, v3
	v_mul_f32_e32 v4, v206, v4
	v_mul_f32_e32 v5, v207, v5
	v_log_f32_e32 v2, v2
	v_log_f32_e32 v3, v3
	v_log_f32_e32 v4, v4
	v_log_f32_e32 v5, v5
	s_waitcnt lgkmcnt(0)
	v_fmac_f32_e32 v201, v2, v236
	v_fmac_f32_e32 v201, v3, v237
	v_fmac_f32_e32 v201, v4, v238
	v_fmac_f32_e32 v201, v5, v239
	v_mfma_scale_f32_32x32x64_f8f6f4 v[18:33], v[74:81], v[154:161], v[18:33], v203, v203 op_sel_hi:[0,0,0]
	ds_read_b128 v[236:239], v202 offset:16
	v_exp_f32_e64 v6, -v6
	v_exp_f32_e64 v7, -v7
	v_exp_f32_e64 v8, -v8
	v_exp_f32_e64 v9, -v9
	v_add_co_u32_e64 v200, s[42:43], v200, v200
	v_add_co_u32_e64 v200, s[48:49], v200, v200
	v_add_co_u32_e64 v200, s[50:51], v200, v200
	v_add_co_u32_e64 v200, s[56:57], v200, v200
	v_add_f32_e32 v6, v6, v166
	v_add_f32_e32 v7, v7, v167
	v_add_f32_e32 v8, v8, v168
	v_add_f32_e32 v9, v9, v169
	v_cndmask_b32_e64 v6, 1.0, v6, s[42:43]
	v_cndmask_b32_e64 v7, 1.0, v7, s[48:49]
	v_cndmask_b32_e64 v8, 1.0, v8, s[50:51]
	v_cndmask_b32_e64 v9, 1.0, v9, s[56:57]
	v_mul_f32_e32 v6, v208, v6
	v_mul_f32_e32 v7, v209, v7
	v_mul_f32_e32 v8, v210, v8
	v_mul_f32_e32 v9, v211, v9
	v_log_f32_e32 v6, v6
	v_log_f32_e32 v7, v7
	v_log_f32_e32 v8, v8
	v_log_f32_e32 v9, v9
	s_waitcnt lgkmcnt(0)
	v_fmac_f32_e32 v201, v6, v236
	v_fmac_f32_e32 v201, v7, v237
	v_fmac_f32_e32 v201, v8, v238
	v_fmac_f32_e32 v201, v9, v239
	v_mfma_scale_f32_32x32x64_f8f6f4 v[18:33], v[82:89], v[138:145], v[18:33], v203, v203 op_sel_hi:[0,0,0]
	ds_read_b128 v[236:239], v202 offset:32
	v_exp_f32_e64 v10, -v10
	v_exp_f32_e64 v11, -v11
	v_exp_f32_e64 v12, -v12
	v_exp_f32_e64 v13, -v13
	v_add_co_u32_e64 v200, s[42:43], v200, v200
	v_add_co_u32_e64 v200, s[48:49], v200, v200
	v_add_co_u32_e64 v200, s[50:51], v200, v200
	v_add_co_u32_e64 v200, s[56:57], v200, v200
	v_add_f32_e32 v10, v10, v170
	v_add_f32_e32 v11, v11, v171
	v_add_f32_e32 v12, v12, v172
	v_add_f32_e32 v13, v13, v173
	v_cndmask_b32_e64 v10, 1.0, v10, s[42:43]
	v_cndmask_b32_e64 v11, 1.0, v11, s[48:49]
	v_cndmask_b32_e64 v12, 1.0, v12, s[50:51]
	v_cndmask_b32_e64 v13, 1.0, v13, s[56:57]
	v_mul_f32_e32 v10, v212, v10
	v_mul_f32_e32 v11, v213, v11
	v_mul_f32_e32 v12, v214, v12
	v_mul_f32_e32 v13, v215, v13
	v_log_f32_e32 v10, v10
	v_log_f32_e32 v11, v11
	v_log_f32_e32 v12, v12
	v_log_f32_e32 v13, v13
	s_waitcnt lgkmcnt(0)
	v_fmac_f32_e32 v201, v10, v236
	v_fmac_f32_e32 v201, v11, v237
	v_fmac_f32_e32 v201, v12, v238
	v_fmac_f32_e32 v201, v13, v239
	v_mfma_scale_f32_32x32x64_f8f6f4 v[18:33], v[90:97], v[130:137], v[18:33], v203, v203 op_sel_hi:[0,0,0]
	s_add_i32 s34, s54, 1
	s_and_b32 s34, s34, 15
	s_lshl_b32 s34, s34, 3
	s_add_i32 s34, s34, s52
	s_lshl_b32 s34, s34, 13
	s_add_i32 s34, s34, s53
	buffer_load_dwordx4 v[146:149], v195, s[44:47], s34 offen
	s_or_b32 s42, s34, 0x400
	buffer_load_dwordx4 v[150:153], v195, s[44:47], s42 offen
	s_or_b32 s43, s34, 0x800
	buffer_load_dwordx4 v[154:157], v195, s[44:47], s43 offen
	s_or_b32 s42, s34, 0xc00
	buffer_load_dwordx4 v[158:161], v195, s[44:47], s42 offen
	s_or_b32 s43, s34, 0x1000
	buffer_load_dwordx4 v[138:141], v195, s[44:47], s43 offen
	s_or_b32 s42, s34, 0x1400
	buffer_load_dwordx4 v[142:145], v195, s[44:47], s42 offen
	s_or_b32 s43, s34, 0x1800
	buffer_load_dwordx4 v[130:133], v195, s[44:47], s43 offen
	s_or_b32 s42, s34, 0x1c00
	buffer_load_dwordx4 v[134:137], v195, s[44:47], s42 offen
	ds_read_b128 v[236:239], v202 offset:48
	v_exp_f32_e64 v14, -v14
	v_exp_f32_e64 v15, -v15
	v_exp_f32_e64 v16, -v16
	v_exp_f32_e64 v17, -v17
	v_add_co_u32_e64 v200, s[42:43], v200, v200
	v_add_co_u32_e64 v200, s[48:49], v200, v200
	v_add_co_u32_e64 v200, s[50:51], v200, v200
	v_add_co_u32_e64 v200, s[56:57], v200, v200
	v_add_f32_e32 v14, v14, v174
	v_add_f32_e32 v15, v15, v175
	v_add_f32_e32 v16, v16, v176
	v_add_f32_e32 v17, v17, v177
	v_cndmask_b32_e64 v14, 1.0, v14, s[42:43]
	v_cndmask_b32_e64 v15, 1.0, v15, s[48:49]
	v_cndmask_b32_e64 v16, 1.0, v16, s[50:51]
	v_cndmask_b32_e64 v17, 1.0, v17, s[56:57]
	v_mul_f32_e32 v14, v216, v14
	v_mul_f32_e32 v15, v217, v15
	v_mul_f32_e32 v16, v218, v16
	v_mul_f32_e32 v17, v219, v17
	v_log_f32_e32 v14, v14
	v_log_f32_e32 v15, v15
	v_log_f32_e32 v16, v16
	v_log_f32_e32 v17, v17
	s_waitcnt lgkmcnt(0)
	v_fmac_f32_e32 v201, v14, v236
	v_fmac_f32_e32 v201, v15, v237
	v_fmac_f32_e32 v201, v16, v238
	v_fmac_f32_e32 v201, v17, v239
	s_cmp_lg_u32 s55, s40
	s_cbranch_scc1 .Lq2_nd1_3
	s_nop 15
	s_nop 7
	v_cndmask_b32_e64 v18, v18, v199, s[0:1]
	v_cndmask_b32_e64 v19, v19, v199, s[2:3]
	v_cndmask_b32_e64 v20, v20, v199, s[4:5]
	v_cndmask_b32_e64 v21, v21, v199, s[6:7]
	v_cndmask_b32_e64 v22, v22, v199, s[8:9]
	v_cndmask_b32_e64 v23, v23, v199, s[10:11]
	v_cndmask_b32_e64 v24, v24, v199, s[12:13]
	v_cndmask_b32_e64 v25, v25, v199, s[14:15]
	v_cndmask_b32_e64 v26, v26, v199, s[16:17]
	v_cndmask_b32_e64 v27, v27, v199, s[18:19]
	v_cndmask_b32_e64 v28, v28, v199, s[20:21]
	v_cndmask_b32_e64 v29, v29, v199, s[22:23]
	v_cndmask_b32_e64 v30, v30, v199, s[24:25]
	v_cndmask_b32_e64 v31, v31, v199, s[26:27]
	v_cndmask_b32_e64 v32, v32, v199, s[28:29]
	v_cndmask_b32_e64 v33, v33, v199, s[30:31]
.Lq2_nd1_3:
	s_nop 3
	s_waitcnt vmcnt(14)
	v_mfma_scale_f32_32x32x64_f8f6f4 v[2:17], v[34:41], v[106:113], 0, v203, v203 op_sel_hi:[0,0,0]
	ds_read_b128 v[236:239], v202 offset:64
	v_exp_f32_e64 v18, -v18
	v_exp_f32_e64 v19, -v19
	v_exp_f32_e64 v20, -v20
	v_exp_f32_e64 v21, -v21
	v_add_co_u32_e64 v200, s[42:43], v200, v200
	v_add_co_u32_e64 v200, s[48:49], v200, v200
	v_add_co_u32_e64 v200, s[50:51], v200, v200
	v_add_co_u32_e64 v200, s[56:57], v200, v200
	v_add_f32_e32 v18, v18, v178
	v_add_f32_e32 v19, v19, v179
	v_add_f32_e32 v20, v20, v180
	v_add_f32_e32 v21, v21, v181
	v_cndmask_b32_e64 v18, 1.0, v18, s[42:43]
	v_cndmask_b32_e64 v19, 1.0, v19, s[48:49]
	v_cndmask_b32_e64 v20, 1.0, v20, s[50:51]
	v_cndmask_b32_e64 v21, 1.0, v21, s[56:57]
	v_mul_f32_e32 v18, v220, v18
	v_mul_f32_e32 v19, v221, v19
	v_mul_f32_e32 v20, v222, v20
	v_mul_f32_e32 v21, v223, v21
	v_log_f32_e32 v18, v18
	v_log_f32_e32 v19, v19
	v_log_f32_e32 v20, v20
	v_log_f32_e32 v21, v21
	s_waitcnt lgkmcnt(0)
	v_fmac_f32_e32 v201, v18, v236
	v_fmac_f32_e32 v201, v19, v237
	v_fmac_f32_e32 v201, v20, v238
	v_fmac_f32_e32 v201, v21, v239
	s_waitcnt vmcnt(12)
	v_mfma_scale_f32_32x32x64_f8f6f4 v[2:17], v[42:49], v[122:129], v[2:17], v203, v203 op_sel_hi:[0,0,0]
	ds_read_b128 v[236:239], v202 offset:80
	v_exp_f32_e64 v22, -v22
	v_exp_f32_e64 v23, -v23
	v_exp_f32_e64 v24, -v24
	v_exp_f32_e64 v25, -v25
	v_add_co_u32_e64 v200, s[42:43], v200, v200
	v_add_co_u32_e64 v200, s[48:49], v200, v200
	v_add_co_u32_e64 v200, s[50:51], v200, v200
	v_add_co_u32_e64 v200, s[56:57], v200, v200
	v_add_f32_e32 v22, v22, v182
	v_add_f32_e32 v23, v23, v183
	v_add_f32_e32 v24, v24, v184
	v_add_f32_e32 v25, v25, v185
	v_cndmask_b32_e64 v22, 1.0, v22, s[42:43]
	v_cndmask_b32_e64 v23, 1.0, v23, s[48:49]
	v_cndmask_b32_e64 v24, 1.0, v24, s[50:51]
	v_cndmask_b32_e64 v25, 1.0, v25, s[56:57]
	v_mul_f32_e32 v22, v224, v22
	v_mul_f32_e32 v23, v225, v23
	v_mul_f32_e32 v24, v226, v24
	v_mul_f32_e32 v25, v227, v25
	v_log_f32_e32 v22, v22
	v_log_f32_e32 v23, v23
	v_log_f32_e32 v24, v24
	v_log_f32_e32 v25, v25
	s_waitcnt lgkmcnt(0)
	v_fmac_f32_e32 v201, v22, v236
	v_fmac_f32_e32 v201, v23, v237
	v_fmac_f32_e32 v201, v24, v238
	v_fmac_f32_e32 v201, v25, v239
	s_waitcnt vmcnt(10)
	v_mfma_scale_f32_32x32x64_f8f6f4 v[2:17], v[50:57], v[114:121], v[2:17], v203, v203 op_sel_hi:[0,0,0]
	ds_read_b128 v[236:239], v202 offset:96
	v_exp_f32_e64 v26, -v26
	v_exp_f32_e64 v27, -v27
	v_exp_f32_e64 v28, -v28
	v_exp_f32_e64 v29, -v29
	v_add_co_u32_e64 v200, s[42:43], v200, v200
	v_add_co_u32_e64 v200, s[48:49], v200, v200
	v_add_co_u32_e64 v200, s[50:51], v200, v200
	v_add_co_u32_e64 v200, s[56:57], v200, v200
	v_add_f32_e32 v26, v26, v186
	v_add_f32_e32 v27, v27, v187
	v_add_f32_e32 v28, v28, v188
	v_add_f32_e32 v29, v29, v189
	v_cndmask_b32_e64 v26, 1.0, v26, s[42:43]
	v_cndmask_b32_e64 v27, 1.0, v27, s[48:49]
	v_cndmask_b32_e64 v28, 1.0, v28, s[50:51]
	v_cndmask_b32_e64 v29, 1.0, v29, s[56:57]
	v_mul_f32_e32 v26, v228, v26
	v_mul_f32_e32 v27, v229, v27
	v_mul_f32_e32 v28, v230, v28
	v_mul_f32_e32 v29, v231, v29
	v_log_f32_e32 v26, v26
	v_log_f32_e32 v27, v27
	v_log_f32_e32 v28, v28
	v_log_f32_e32 v29, v29
	s_waitcnt lgkmcnt(0)
	v_fmac_f32_e32 v201, v26, v236
	v_fmac_f32_e32 v201, v27, v237
	v_fmac_f32_e32 v201, v28, v238
	v_fmac_f32_e32 v201, v29, v239
	s_waitcnt vmcnt(8)
	v_mfma_scale_f32_32x32x64_f8f6f4 v[2:17], v[58:65], v[98:105], v[2:17], v203, v203 op_sel_hi:[0,0,0]
	ds_read_b128 v[236:239], v202 offset:112
	v_exp_f32_e64 v30, -v30
	v_exp_f32_e64 v31, -v31
	v_exp_f32_e64 v32, -v32
	v_exp_f32_e64 v33, -v33
	v_add_co_u32_e64 v200, s[42:43], v200, v200
	v_add_co_u32_e64 v200, s[48:49], v200, v200
	v_add_co_u32_e64 v200, s[50:51], v200, v200
	v_add_co_u32_e64 v200, s[56:57], v200, v200
	v_add_f32_e32 v30, v30, v190
	v_add_f32_e32 v31, v31, v191
	v_add_f32_e32 v32, v32, v192
	v_add_f32_e32 v33, v33, v193
	v_cndmask_b32_e64 v30, 1.0, v30, s[42:43]
	v_cndmask_b32_e64 v31, 1.0, v31, s[48:49]
	v_cndmask_b32_e64 v32, 1.0, v32, s[50:51]
	v_cndmask_b32_e64 v33, 1.0, v33, s[56:57]
	v_mul_f32_e32 v30, v232, v30
	v_mul_f32_e32 v31, v233, v31
	v_mul_f32_e32 v32, v234, v32
	v_mul_f32_e32 v33, v235, v33
	v_log_f32_e32 v30, v30
	v_log_f32_e32 v31, v31
	v_log_f32_e32 v32, v32
	v_log_f32_e32 v33, v33
	s_waitcnt lgkmcnt(0)
	v_fmac_f32_e32 v201, v30, v236
	v_fmac_f32_e32 v201, v31, v237
	v_fmac_f32_e32 v201, v32, v238
	v_fmac_f32_e32 v201, v33, v239
	s_add_i32 s39, s39, 1
	s_cmp_lt_u32 s39, 4
	s_cbranch_scc1 .Lq2_loop
